# final_output_stores_nontemporal
# speedup vs baseline: 1.0089x; 1.0089x over previous
.Lfin_rounds_done:
	v_mul_f32_e32 v94, v33, v33
	v_mul_f32_e32 v95, v35, v35
	v_mul_f32_e32 v96, v37, v37
	v_mul_f32_e32 v97, v39, v39
	v_mul_f32_e32 v98, v41, v41
	v_mul_f32_e32 v99, v43, v43
	v_mul_f32_e32 v100, v45, v45
	v_mul_f32_e32 v101, v47, v47
	v_fmac_f32_e32 v94, v32, v32
	v_fmac_f32_e32 v95, v34, v34
	v_fmac_f32_e32 v96, v36, v36
	v_fmac_f32_e32 v97, v38, v38
	v_fmac_f32_e32 v98, v40, v40
	v_fmac_f32_e32 v99, v42, v42
	v_fmac_f32_e32 v100, v44, v44
	v_fmac_f32_e32 v101, v46, v46
	v_add_f32_e32 v94, v94, v95
	v_add_f32_e32 v96, v96, v97
	v_add_f32_e32 v98, v98, v99
	v_add_f32_e32 v100, v100, v101
	v_add_f32_e32 v84, v96, v94
	v_add_f32_e32 v84, v98, v84
	v_add_f32_e32 v84, v100, v84
	s_lshl_b32 s10, s2, 12
	s_add_u32 s10, s24, s10
	s_addc_u32 s11, s25, 0
	s_nop 1
	v_add_f32_dpp v84, v84, v84 quad_perm:[1,0,3,2] row_mask:0xf bank_mask:0xf bound_ctrl:1
	s_nop 1
	v_add_f32_dpp v84, v84, v84 quad_perm:[2,3,0,1] row_mask:0xf bank_mask:0xf bound_ctrl:1
	s_nop 1
	v_add_f32_dpp v84, v84, v84 row_half_mirror row_mask:0xf bank_mask:0xf bound_ctrl:1
	s_nop 1
	v_add_f32_dpp v84, v84, v84 row_mirror row_mask:0xf bank_mask:0xf bound_ctrl:1
	v_mov_b32_e32 v85, v84
	s_nop 1
	v_permlane16_swap_b32_e32 v84, v85
	v_add_f32_e32 v84, v84, v85
	v_mov_b32_e32 v85, v84
	s_nop 1
	v_permlane32_swap_b32_e32 v84, v85
	v_add_f32_e32 v84, v84, v85
	v_fmamk_f32 v84, v84, 0x3a800000, v108
	v_mul_f32_e32 v85, 0x4f800000, v84
	v_cmp_gt_f32_e32 vcc, s35, v84
	s_nop 1
	v_cndmask_b32_e32 v84, v84, v85, vcc
	v_sqrt_f32_e32 v85, v84
	s_nop 0
	v_add_u32_e32 v86, -1, v85
	v_add_u32_e32 v91, 1, v85
	v_fma_f32 v89, -v86, v85, v84
	v_fma_f32 v90, -v91, v85, v84
	v_cmp_ge_f32_e64 s[12:13], 0, v89
	s_nop 1
	v_cndmask_b32_e64 v85, v85, v86, s[12:13]
	v_cmp_lt_f32_e64 s[12:13], 0, v90
	s_nop 1
	v_cndmask_b32_e64 v85, v85, v91, s[12:13]
	v_mul_f32_e32 v86, 0x37800000, v85
	v_cndmask_b32_e32 v85, v85, v86, vcc
	v_cmp_class_f32_e32 vcc, v84, v109
	s_nop 1
	v_cndmask_b32_e32 v84, v85, v84, vcc
	v_div_scale_f32 v88, s[12:13], v84, v84, 1.0
	v_rcp_f32_e32 v89, v88
	v_div_scale_f32 v90, vcc, 1.0, v84, 1.0
	s_nop 0
	v_fma_f32 v91, -v88, v89, 1.0
	v_fmac_f32_e32 v89, v91, v89
	v_mul_f32_e32 v91, v90, v89
	v_fma_f32 v92, -v88, v91, v90
	v_fmac_f32_e32 v91, v92, v89
	v_fma_f32 v88, -v88, v91, v90
	v_div_fmas_f32 v88, v88, v89, v91
	v_div_fixup_f32 v88, v88, v84, 1.0
	v_pk_mul_f32 v[32:33], v[88:89], v[32:33] op_sel_hi:[0,1]
	v_pk_mul_f32 v[34:35], v[88:89], v[34:35] op_sel_hi:[0,1]
	v_pk_mul_f32 v[36:37], v[88:89], v[36:37] op_sel_hi:[0,1]
	v_pk_mul_f32 v[38:39], v[88:89], v[38:39] op_sel_hi:[0,1]
	v_pk_mul_f32 v[40:41], v[88:89], v[40:41] op_sel_hi:[0,1]
	v_pk_mul_f32 v[42:43], v[88:89], v[42:43] op_sel_hi:[0,1]
	v_pk_mul_f32 v[44:45], v[88:89], v[44:45] op_sel_hi:[0,1]
	v_pk_mul_f32 v[46:47], v[88:89], v[46:47] op_sel_hi:[0,1]
	v_pk_mul_f32 v[32:33], v[112:113], v[32:33]
	v_pk_mul_f32 v[34:35], v[114:115], v[34:35]
	global_store_dwordx4 v107, v[32:35], s[10:11] nt
	v_pk_mul_f32 v[36:37], v[116:117], v[36:37]
	v_pk_mul_f32 v[38:39], v[118:119], v[38:39]
	global_store_dwordx4 v107, v[36:39], s[10:11] offset:1024 nt
	v_pk_mul_f32 v[40:41], v[120:121], v[40:41]
	v_pk_mul_f32 v[42:43], v[122:123], v[42:43]
	global_store_dwordx4 v107, v[40:43], s[10:11] offset:2048 nt
	v_pk_mul_f32 v[44:45], v[124:125], v[44:45]
	v_pk_mul_f32 v[46:47], v[126:127], v[46:47]
	global_store_dwordx4 v107, v[44:47], s[10:11] offset:3072 nt
	s_cmp_eq_u32 s29, 0
	s_cbranch_scc1 .Lfin_skipB
	v_mul_f32_e32 v94, v49, v49
	v_mul_f32_e32 v95, v51, v51
	v_mul_f32_e32 v96, v53, v53
	v_mul_f32_e32 v97, v55, v55
	v_mul_f32_e32 v98, v57, v57
	v_mul_f32_e32 v99, v59, v59
	v_mul_f32_e32 v100, v61, v61
	v_mul_f32_e32 v101, v63, v63
	v_fmac_f32_e32 v94, v48, v48
	v_fmac_f32_e32 v95, v50, v50
	v_fmac_f32_e32 v96, v52, v52
	v_fmac_f32_e32 v97, v54, v54
	v_fmac_f32_e32 v98, v56, v56
	v_fmac_f32_e32 v99, v58, v58
	v_fmac_f32_e32 v100, v60, v60
	v_fmac_f32_e32 v101, v62, v62
	v_add_f32_e32 v94, v94, v95
	v_add_f32_e32 v96, v96, v97
	v_add_f32_e32 v98, v98, v99
	v_add_f32_e32 v100, v100, v101
	v_add_f32_e32 v84, v96, v94
	v_add_f32_e32 v84, v98, v84
	v_add_f32_e32 v84, v100, v84
	s_lshl_b32 s10, s3, 12
	s_add_u32 s10, s24, s10
	s_addc_u32 s11, s25, 0
	s_nop 1
	v_add_f32_dpp v84, v84, v84 quad_perm:[1,0,3,2] row_mask:0xf bank_mask:0xf bound_ctrl:1
	s_nop 1
	v_add_f32_dpp v84, v84, v84 quad_perm:[2,3,0,1] row_mask:0xf bank_mask:0xf bound_ctrl:1
	s_nop 1
	v_add_f32_dpp v84, v84, v84 row_half_mirror row_mask:0xf bank_mask:0xf bound_ctrl:1
	s_nop 1
	v_add_f32_dpp v84, v84, v84 row_mirror row_mask:0xf bank_mask:0xf bound_ctrl:1
	v_mov_b32_e32 v85, v84
	s_nop 1
	v_permlane16_swap_b32_e32 v84, v85
	v_add_f32_e32 v84, v84, v85
	v_mov_b32_e32 v85, v84
	s_nop 1
	v_permlane32_swap_b32_e32 v84, v85
	v_add_f32_e32 v84, v84, v85
	v_fmamk_f32 v84, v84, 0x3a800000, v108
	v_mul_f32_e32 v85, 0x4f800000, v84
	v_cmp_gt_f32_e32 vcc, s35, v84
	s_nop 1
	v_cndmask_b32_e32 v84, v84, v85, vcc
	v_sqrt_f32_e32 v85, v84
	s_nop 0
	v_add_u32_e32 v86, -1, v85
	v_add_u32_e32 v91, 1, v85
	v_fma_f32 v89, -v86, v85, v84
	v_fma_f32 v90, -v91, v85, v84
	v_cmp_ge_f32_e64 s[12:13], 0, v89
	s_nop 1
	v_cndmask_b32_e64 v85, v85, v86, s[12:13]
	v_cmp_lt_f32_e64 s[12:13], 0, v90
	s_nop 1
	v_cndmask_b32_e64 v85, v85, v91, s[12:13]
	v_mul_f32_e32 v86, 0x37800000, v85
	v_cndmask_b32_e32 v85, v85, v86, vcc
	v_cmp_class_f32_e32 vcc, v84, v109
	s_nop 1
	v_cndmask_b32_e32 v84, v85, v84, vcc
	v_div_scale_f32 v88, s[12:13], v84, v84, 1.0
	v_rcp_f32_e32 v89, v88
	v_div_scale_f32 v90, vcc, 1.0, v84, 1.0
	s_nop 0
	v_fma_f32 v91, -v88, v89, 1.0
	v_fmac_f32_e32 v89, v91, v89
	v_mul_f32_e32 v91, v90, v89
	v_fma_f32 v92, -v88, v91, v90
	v_fmac_f32_e32 v91, v92, v89
	v_fma_f32 v88, -v88, v91, v90
	v_div_fmas_f32 v88, v88, v89, v91
	v_div_fixup_f32 v88, v88, v84, 1.0
	v_pk_mul_f32 v[48:49], v[88:89], v[48:49] op_sel_hi:[0,1]
	v_pk_mul_f32 v[50:51], v[88:89], v[50:51] op_sel_hi:[0,1]
	v_pk_mul_f32 v[52:53], v[88:89], v[52:53] op_sel_hi:[0,1]
	v_pk_mul_f32 v[54:55], v[88:89], v[54:55] op_sel_hi:[0,1]
	v_pk_mul_f32 v[56:57], v[88:89], v[56:57] op_sel_hi:[0,1]
	v_pk_mul_f32 v[58:59], v[88:89], v[58:59] op_sel_hi:[0,1]
	v_pk_mul_f32 v[60:61], v[88:89], v[60:61] op_sel_hi:[0,1]
	v_pk_mul_f32 v[62:63], v[88:89], v[62:63] op_sel_hi:[0,1]
	v_pk_mul_f32 v[48:49], v[112:113], v[48:49]
	v_pk_mul_f32 v[50:51], v[114:115], v[50:51]
	global_store_dwordx4 v107, v[48:51], s[10:11] nt
	v_pk_mul_f32 v[52:53], v[116:117], v[52:53]
	v_pk_mul_f32 v[54:55], v[118:119], v[54:55]
	global_store_dwordx4 v107, v[52:55], s[10:11] offset:1024 nt
	v_pk_mul_f32 v[56:57], v[120:121], v[56:57]
	v_pk_mul_f32 v[58:59], v[122:123], v[58:59]
	global_store_dwordx4 v107, v[56:59], s[10:11] offset:2048 nt
	v_pk_mul_f32 v[60:61], v[124:125], v[60:61]
	v_pk_mul_f32 v[62:63], v[126:127], v[62:63]
	global_store_dwordx4 v107, v[60:63], s[10:11] offset:3072 nt
